# nt (streaming) cache policy on the background MoE-weight-conversion loads in the neighbourhood-attention phase
# baseline (speedup 1.0000x reference)
.LBB0_281:
	s_lshl_b64 s[28:29], s[28:29], 10
	s_add_u32 s28, s44, s28
	s_addc_u32 s29, s45, s29
	v_mad_i64_i32 v[4:5], s[44:45], s46, v209, 0
	s_add_u32 s28, s28, s12
	v_lshl_add_u64 v[4:5], v[4:5], 2, s[42:43]
	v_lshlrev_b32_e32 v2, 2, v210
	s_addc_u32 s29, s29, s13
	v_lshl_add_u64 v[4:5], v[4:5], 0, v[2:3]
	s_lshl_b32 s12, s46, 4
	v_lshl_add_u64 v[6:7], v[4:5], 0, s[12:13]
	global_load_dwordx4 v[134:137], v[4:5], off nt
	global_load_dwordx4 v[130:133], v[6:7], off nt
	v_lshl_add_u64 v[4:5], v[6:7], 0, s[12:13]
	v_lshl_add_u64 v[6:7], v[4:5], 0, s[12:13]
	global_load_dwordx4 v[142:145], v[4:5], off nt
	global_load_dwordx4 v[138:141], v[6:7], off nt
	v_lshl_add_u64 v[4:5], v[6:7], 0, s[12:13]
	v_lshl_add_u64 v[6:7], v[4:5], 0, s[12:13]
	global_load_dwordx4 v[150:153], v[4:5], off nt
	global_load_dwordx4 v[146:149], v[6:7], off nt
	v_lshl_add_u64 v[4:5], v[6:7], 0, s[12:13]
	v_lshl_add_u64 v[6:7], v[4:5], 0, s[12:13]
	global_load_dwordx4 v[158:161], v[4:5], off nt
	global_load_dwordx4 v[154:157], v[6:7], off nt
	s_add_i32 s64, s64, s34
	s_movk_i32 s65, 0x400

.LBB0_328:
	s_lshl_b64 s[18:19], s[18:19], 10
	s_add_u32 s18, s40, s18
	s_addc_u32 s19, s41, s19
	v_mad_i64_i32 v[52:53], s[40:41], s42, v209, 0
	s_add_u32 s18, s18, s12
	v_lshl_add_u64 v[52:53], v[52:53], 2, s[38:39]
	v_lshlrev_b32_e32 v2, 2, v210
	s_addc_u32 s19, s19, s13
	v_lshl_add_u64 v[52:53], v[52:53], 0, v[2:3]
	s_lshl_b32 s12, s42, 4
	v_lshl_add_u64 v[54:55], v[52:53], 0, s[12:13]
	global_load_dwordx4 v[98:101], v[52:53], off nt
	global_load_dwordx4 v[102:105], v[54:55], off nt
	v_lshl_add_u64 v[52:53], v[54:55], 0, s[12:13]
	v_lshl_add_u64 v[54:55], v[52:53], 0, s[12:13]
	global_load_dwordx4 v[106:109], v[52:53], off nt
	global_load_dwordx4 v[110:113], v[54:55], off nt
	v_lshl_add_u64 v[52:53], v[54:55], 0, s[12:13]
	v_lshl_add_u64 v[54:55], v[52:53], 0, s[12:13]
	global_load_dwordx4 v[114:117], v[52:53], off nt
	global_load_dwordx4 v[118:121], v[54:55], off nt
	v_lshl_add_u64 v[52:53], v[54:55], 0, s[12:13]
	v_lshl_add_u64 v[54:55], v[52:53], 0, s[12:13]
	global_load_dwordx4 v[122:125], v[52:53], off nt
	global_load_dwordx4 v[126:129], v[54:55], off nt
	s_add_i32 s62, s62, s34
	s_movk_i32 s63, 0x400

.LBB0_355:
	s_lshl_b64 s[14:15], s[14:15], 10
	s_add_u32 s5, s18, s14
	s_addc_u32 s12, s19, s15
	v_mad_i64_i32 v[22:23], s[14:15], s20, v209, 0
	s_add_u32 s28, s5, s3
	v_lshl_add_u64 v[22:23], v[22:23], 2, s[16:17]
	v_lshlrev_b32_e32 v2, 2, v210
	s_addc_u32 s29, s12, s13
	v_lshl_add_u64 v[22:23], v[22:23], 0, v[2:3]
	s_lshl_b32 s12, s20, 4
	v_lshl_add_u64 v[24:25], v[22:23], 0, s[12:13]
	global_load_dwordx4 v[134:137], v[22:23], off nt
	global_load_dwordx4 v[130:133], v[24:25], off nt
	v_lshl_add_u64 v[22:23], v[24:25], 0, s[12:13]
	v_lshl_add_u64 v[24:25], v[22:23], 0, s[12:13]
	global_load_dwordx4 v[142:145], v[22:23], off nt
	global_load_dwordx4 v[138:141], v[24:25], off nt
	v_lshl_add_u64 v[22:23], v[24:25], 0, s[12:13]
	v_lshl_add_u64 v[24:25], v[22:23], 0, s[12:13]
	global_load_dwordx4 v[150:153], v[22:23], off nt
	global_load_dwordx4 v[146:149], v[24:25], off nt
	v_lshl_add_u64 v[22:23], v[24:25], 0, s[12:13]
	v_lshl_add_u64 v[24:25], v[22:23], 0, s[12:13]
	global_load_dwordx4 v[158:161], v[22:23], off nt
	global_load_dwordx4 v[154:157], v[24:25], off nt
	s_add_i32 s64, s64, s34
	s_movk_i32 s65, 0x400
